# baseline (speedup 1.0000x reference)
_Z6k_agg1PKiS0_PK6__halfPKfS5_S5_S3_S5_S5_PS1_PfS7_S5_S0_S0_:
	s_and_b32 s3, s2, 7
	s_mul_i32 s5, s3, 0x30d
	s_min_u32 s3, s3, 2
	s_lshr_b32 s2, s2, 3
	v_readfirstlane_b32 s36, v0
	s_add_i32 s2, s3, s2
	s_lshr_b32 s4, s36, 6
	s_add_i32 s2, s2, s5
	s_load_dwordx4 s[8:11], s[0:1], 0x60
	s_lshl_b32 s33, s2, 4
	s_lshl_b32 s2, s4, 2
	v_bfe_u32 v42, v0, 4, 2
	s_add_i32 s2, s2, s33
	v_or_b32_e32 v2, s2, v42
	v_ashrrev_i32_e32 v3, 31, v2
	v_lshlrev_b64 v[10:11], 2, v[2:3]
	s_load_dwordx2 s[2:3], s[0:1], 0x70
	s_waitcnt lgkmcnt(0)
	v_lshl_add_u64 v[2:3], s[10:11], 0, v[10:11]
	global_load_dword v1, v[2:3], off
	s_load_dwordx2 s[6:7], s[0:1], 0x20
	s_load_dwordx2 s[26:27], s[0:1], 0x8
	v_and_b32_e32 v44, 15, v0
	v_lshlrev_b32_e32 v12, 5, v44
	v_lshl_add_u64 v[10:11], s[2:3], 0, v[10:11]
	global_load_dwordx4 v[2:5], v12, s[8:9] offset:16
	global_load_dwordx4 v[6:9], v12, s[8:9]
	global_load_dword v48, v[10:11], off
	v_mov_b32_e32 v33, 0
	v_and_b32_e32 v32, 12, v0
	v_mov_b32_e32 v52, 0
	s_waitcnt vmcnt(3)
	v_ashrrev_i32_e32 v46, 24, v1
	v_add_u32_e32 v10, s33, v46
	v_ashrrev_i32_e32 v11, 31, v10
	s_waitcnt lgkmcnt(0)
	v_lshl_add_u64 v[10:11], v[10:11], 4, s[6:7]
	v_lshl_add_u64 v[10:11], v[10:11], 0, v[32:33]
	global_load_dword v50, v[10:11], off
	v_and_b32_e32 v51, 0xffffff, v1
	v_add_u32_e32 v1, v51, v44
	s_waitcnt vmcnt(1)
	v_cmp_lt_i32_e32 vcc, v1, v48
	s_and_saveexec_b64 s[2:3], vcc
	s_cbranch_execz .LBB3_2
	v_lshlrev_b32_e32 v1, 2, v1
	global_load_dword v52, v1, s[26:27] nt

.LBB3_8:
	v_lshl_add_u64 v[0:1], v[40:41], 2, s[26:27]
	global_load_dword v52, v[0:1], off offset:64 nt
	s_or_b64 exec, exec, s[4:5]
	v_cmp_lt_i32_e64 s[2:3], 0, v59
	s_and_saveexec_b64 s[34:35], s[2:3]
	s_cbranch_execz .LBB3_7
